# speedup vs baseline: 1.0963x; 1.0018x over previous
.LBB1_11:
	s_or_b64 exec, exec, s[28:29]
	s_add_i32 s28, s22, 1
	s_ashr_i32 s29, s28, 31
	s_lshl_b64 s[28:29], s[28:29], 7
	s_add_u32 s50, s43, s28
	s_addc_u32 s51, s44, s29
	v_lshl_add_u64 v[0:1], s[50:51], 0, v[128:129]
	v_readfirstlane_b32 s43, v177
	v_lshl_add_u64 v[2:3], v[0:1], 0, v[134:135]
	s_mov_b32 m0, s43
	v_readfirstlane_b32 s43, v178
	s_add_u32 s44, s45, s28
	s_waitcnt vmcnt(4)
	s_barrier
	global_load_lds_dwordx4 v[2:3], off
	v_lshl_add_u64 v[0:1], v[0:1], 0, v[136:137]
	s_mov_b32 m0, s43
	s_addc_u32 s45, s46, s29
	global_load_lds_dwordx4 v[0:1], off
	v_lshl_add_u64 v[0:1], s[44:45], 0, v[128:129]
	v_readfirstlane_b32 s43, v167
	v_lshl_add_u64 v[2:3], v[0:1], 0, v[134:135]
	s_mov_b32 m0, s43
	v_readfirstlane_b32 s43, v168
	s_add_u32 s28, s47, s28
	global_load_lds_dwordx4 v[2:3], off
	v_lshl_add_u64 v[0:1], v[0:1], 0, v[136:137]
	s_mov_b32 m0, s43
	s_addc_u32 s29, s48, s29
	global_load_lds_dwordx4 v[0:1], off
	v_lshl_add_u64 v[0:1], s[28:29], 0, v[128:129]
	v_readfirstlane_b32 s28, v179
	v_add_u32_e32 v146, 0x2000, v179
	v_lshl_add_u64 v[2:3], v[0:1], 0, v[134:135]
	s_mov_b32 m0, s28
	v_readfirstlane_b32 s28, v146
	global_load_lds_dwordx4 v[2:3], off
	v_lshl_add_u64 v[0:1], v[0:1], 0, v[136:137]
	s_mov_b32 m0, s28
	v_mov_b32_e32 v127, 0
	global_load_lds_dwordx4 v[0:1], off
	s_cmp_lt_i32 s41, 3
	v_mov_b32_e32 v126, v127
	v_mov_b32_e32 v125, v127
	v_mov_b32_e32 v124, v127
	v_mov_b32_e32 v123, v127
	v_mov_b32_e32 v122, v127
	v_mov_b32_e32 v121, v127
	v_mov_b32_e32 v120, v127
	v_mov_b32_e32 v119, v127
	v_mov_b32_e32 v118, v127
	v_mov_b32_e32 v117, v127
	v_mov_b32_e32 v116, v127
	v_mov_b32_e32 v115, v127
	v_mov_b32_e32 v114, v127
	v_mov_b32_e32 v113, v127
	v_mov_b32_e32 v112, v127
	v_mov_b32_e32 v111, v127
	v_mov_b32_e32 v110, v127
	v_mov_b32_e32 v109, v127
	v_mov_b32_e32 v108, v127
	v_mov_b32_e32 v107, v127
	v_mov_b32_e32 v106, v127
	v_mov_b32_e32 v105, v127
	v_mov_b32_e32 v104, v127
	v_mov_b32_e32 v103, v127
	v_mov_b32_e32 v102, v127
	v_mov_b32_e32 v101, v127
	v_mov_b32_e32 v100, v127
	v_mov_b32_e32 v99, v127
	v_mov_b32_e32 v98, v127
	v_mov_b32_e32 v97, v127
	v_mov_b32_e32 v96, v127
	v_mov_b32_e32 v95, v127
	v_mov_b32_e32 v94, v127
	v_mov_b32_e32 v93, v127
	v_mov_b32_e32 v92, v127
	v_mov_b32_e32 v91, v127
	v_mov_b32_e32 v90, v127
	v_mov_b32_e32 v89, v127
	v_mov_b32_e32 v88, v127
	v_mov_b32_e32 v87, v127
	v_mov_b32_e32 v86, v127
	v_mov_b32_e32 v85, v127
	v_mov_b32_e32 v84, v127
	v_mov_b32_e32 v83, v127
	v_mov_b32_e32 v82, v127
	v_mov_b32_e32 v81, v127
	v_mov_b32_e32 v80, v127
	v_mov_b32_e32 v79, v127
	v_mov_b32_e32 v78, v127
	v_mov_b32_e32 v77, v127
	v_mov_b32_e32 v76, v127
	v_mov_b32_e32 v75, v127
	v_mov_b32_e32 v74, v127
	v_mov_b32_e32 v73, v127
	v_mov_b32_e32 v72, v127
	v_mov_b32_e32 v71, v127
	v_mov_b32_e32 v70, v127
	v_mov_b32_e32 v69, v127
	v_mov_b32_e32 v68, v127
	v_mov_b32_e32 v67, v127
	v_mov_b32_e32 v66, v127
	v_mov_b32_e32 v65, v127
	v_mov_b32_e32 v64, v127
	v_mov_b32_e32 v63, v127
	v_mov_b32_e32 v62, v127
	v_mov_b32_e32 v61, v127
	v_mov_b32_e32 v60, v127
	v_mov_b32_e32 v59, v127
	v_mov_b32_e32 v58, v127
	v_mov_b32_e32 v57, v127
	v_mov_b32_e32 v56, v127
	v_mov_b32_e32 v55, v127
	v_mov_b32_e32 v54, v127
	v_mov_b32_e32 v53, v127
	v_mov_b32_e32 v52, v127
	v_mov_b32_e32 v51, v127
	v_mov_b32_e32 v50, v127
	v_mov_b32_e32 v49, v127
	v_mov_b32_e32 v48, v127
	v_mov_b32_e32 v47, v127
	v_mov_b32_e32 v46, v127
	v_mov_b32_e32 v45, v127
	v_mov_b32_e32 v44, v127
	v_mov_b32_e32 v43, v127
	v_mov_b32_e32 v42, v127
	v_mov_b32_e32 v41, v127
	v_mov_b32_e32 v40, v127
	v_mov_b32_e32 v39, v127
	v_mov_b32_e32 v38, v127
	v_mov_b32_e32 v37, v127
	v_mov_b32_e32 v36, v127
	v_mov_b32_e32 v35, v127
	v_mov_b32_e32 v34, v127
	v_mov_b32_e32 v33, v127
	v_mov_b32_e32 v32, v127
	v_mov_b32_e32 v31, v127
	v_mov_b32_e32 v30, v127
	v_mov_b32_e32 v29, v127
	v_mov_b32_e32 v28, v127
	v_mov_b32_e32 v27, v127
	v_mov_b32_e32 v26, v127
	v_mov_b32_e32 v25, v127
	v_mov_b32_e32 v24, v127
	v_mov_b32_e32 v23, v127
	v_mov_b32_e32 v22, v127
	v_mov_b32_e32 v21, v127
	v_mov_b32_e32 v20, v127
	v_mov_b32_e32 v19, v127
	v_mov_b32_e32 v18, v127
	v_mov_b32_e32 v17, v127
	v_mov_b32_e32 v16, v127
	v_mov_b32_e32 v15, v127
	v_mov_b32_e32 v14, v127
	v_mov_b32_e32 v13, v127
	v_mov_b32_e32 v12, v127
	v_mov_b32_e32 v11, v127
	v_mov_b32_e32 v10, v127
	v_mov_b32_e32 v9, v127
	v_mov_b32_e32 v8, v127
	v_mov_b32_e32 v7, v127
	v_mov_b32_e32 v6, v127
	v_mov_b32_e32 v5, v127
	v_mov_b32_e32 v4, v127
	v_mov_b32_e32 v3, v127
	v_mov_b32_e32 v2, v127
	v_mov_b32_e32 v1, v127
	v_mov_b32_e32 v0, v127
	s_waitcnt vmcnt(6)
	s_barrier
	s_cbranch_scc1 .LBB1_14
	s_lshl_b64 s[28:29], s[4:5], 12
	s_lshl_b64 s[44:45], s[20:21], 12
	s_lshl_b64 s[24:25], s[24:25], 12
	s_lshl_b64 s[26:27], s[26:27], 12
	s_add_i32 s5, s41, -2
	v_lshl_add_u64 v[138:139], s[26:27], 1, v[130:131]
	v_lshl_add_u64 v[140:141], s[28:29], 1, v[132:133]
	v_lshl_add_u64 v[142:143], s[44:45], 1, v[130:131]
	v_lshl_add_u64 v[144:145], s[24:25], 1, v[132:133]
	s_mov_b32 s21, 0
